# MoE unit dealing (P6, P7): every full round dealt statically, only the last partial round by tickets (one round fewer of per-unit ticket atomics + drains); rest as v52
# speedup vs baseline: 1.0040x; 1.0040x over previous
.LBB0_2239:
	s_add_u32 s22, s90, 0x1c000000
	v_and_b32_e32 v10, 15, v0
	s_addc_u32 s23, s91, 0
	v_lshl_or_b32 v207, s0, 6, v10
	s_lshl_b32 s2, s0, 13
	s_lshl_b32 s0, s1, 5
	s_add_i32 s70, s62, 0x18000
	s_mov_b64 s[24:25], 0x80
	s_and_b32 s30, s0, 0x60
	v_lshl_add_u64 v[8:9], v[8:9], 0, s[24:25]
	s_mov_b32 m0, s70
	s_add_i32 s71, s62, 0x1a000
	s_lshl_b32 s3, s30, 7
	s_waitcnt vmcnt(2)
	s_barrier
	global_load_lds_dwordx4 v[8:9], off
	v_lshl_add_u64 v[6:7], v[6:7], 0, s[24:25]
	s_mov_b32 m0, s71
	s_add_i32 s72, s62, 0x8000
	s_add_i32 s73, s62, 0xa000
	global_load_lds_dwordx4 v[6:7], off
	v_lshl_add_u64 v[2:3], v[2:3], 0, s[24:25]
	s_mov_b32 m0, s72
	s_add_u32 s0, s6, 0x40080
	global_load_lds_dwordx4 v[2:3], off
	v_lshl_add_u64 v[2:3], v[4:5], 0, s[24:25]
	s_mov_b32 m0, s73
	s_addc_u32 s1, s7, 0
	s_add_i32 s74, s62, 0x1c000
	global_load_lds_dwordx4 v[2:3], off
	v_lshl_add_u64 v[2:3], s[0:1], 0, v[200:201]
	s_mov_b32 m0, s74
	s_add_i32 s76, s62, 0x1e000
	global_load_lds_dwordx4 v[2:3], off
	v_lshl_add_u64 v[2:3], s[0:1], 0, v[202:203]
	s_mov_b32 m0, s76
	s_and_b32 s31, s11, 0xc0
	global_load_lds_dwordx4 v[2:3], off
	s_cmpk_lt_u32 s11, 0x100
	s_cselect_b64 s[26:27], -1, 0
	s_ashr_i32 s8, s33, 8
	s_max_i32 s8, s8, 1
	s_add_i32 s8, s8, 0
	s_and_b64 s[4:5], s[4:5], exec
	s_cselect_b32 s77, s8, 2.0
	s_add_i32 s4, 0, 0x22400
	s_lshl_b32 s5, s31, 2
	s_lshl_b32 s11, s77, 8
	s_add_i32 s78, s4, s5
	v_lshl_add_u32 v209, v1, 2, s4
	v_lshl_add_u32 v223, v199, 2, s4
	s_sub_i32 s4, s10, s11
	s_addk_i32 s4, 0x87
	s_ashr_i32 s79, s4, 3
	s_ashr_i32 s4, s97, 5
	s_ashr_i32 s5, s4, 31
	v_and_b32_e32 v12, 48, v0
	v_lshlrev_b32_e32 v13, 2, v0
	v_lshlrev_b32_e32 v3, 6, v0
	s_movk_i32 s0, 0x3c0
	s_lshl_b64 s[8:9], s[4:5], 2
	v_lshl_or_b32 v10, v10, 6, v12
	v_and_b32_e32 v13, 32, v13
	v_and_or_b32 v3, v3, s0, v12
	s_waitcnt vmcnt(6)
	s_add_u32 s28, s90, s8
	v_mov_b32_e32 v68, v67
	v_mov_b32_e32 v69, v67
	v_lshrrev_b32_e32 v11, 1, v0
	v_bitop3_b32 v2, v10, s2, v13 bitop3:0xde
	v_bitop3_b32 v3, s3, v3, v13 bitop3:0xf6
	v_and_b32_e32 v4, 16, v0
	s_addc_u32 s29, s91, s9
	s_mul_i32 s80, s79, s4
	s_add_i32 s4, 0, 0x22100
	v_mov_b32_e32 v66, v67
	v_mov_b64_e32 v[72:73], v[68:69]
	v_mov_b64_e32 v[76:77], v[68:69]
	v_mov_b64_e32 v[80:81], v[68:69]
	v_mov_b64_e32 v[84:85], v[68:69]
	v_mov_b64_e32 v[88:89], v[68:69]
	v_mov_b64_e32 v[92:93], v[68:69]
	v_mov_b64_e32 v[96:97], v[68:69]
	v_mov_b64_e32 v[100:101], v[68:69]
	v_mov_b64_e32 v[104:105], v[68:69]
	v_mov_b64_e32 v[108:109], v[68:69]
	v_mov_b64_e32 v[112:113], v[68:69]
	v_mov_b64_e32 v[116:117], v[68:69]
	v_mov_b64_e32 v[120:121], v[68:69]
	v_mov_b64_e32 v[124:125], v[68:69]
	v_mov_b64_e32 v[128:129], v[68:69]
	v_mov_b64_e32 v[132:133], v[68:69]
	v_mov_b64_e32 v[136:137], v[68:69]
	v_mov_b64_e32 v[140:141], v[68:69]
	v_mov_b64_e32 v[144:145], v[68:69]
	v_mov_b64_e32 v[148:149], v[68:69]
	v_mov_b64_e32 v[152:153], v[68:69]
	v_mov_b64_e32 v[156:157], v[68:69]
	v_mov_b64_e32 v[160:161], v[68:69]
	v_mov_b64_e32 v[164:165], v[68:69]
	v_mov_b64_e32 v[168:169], v[68:69]
	v_mov_b64_e32 v[172:173], v[68:69]
	v_mov_b64_e32 v[176:177], v[68:69]
	v_mov_b64_e32 v[180:181], v[68:69]
	v_mov_b64_e32 v[184:185], v[68:69]
	v_mov_b64_e32 v[188:189], v[68:69]
	v_mov_b64_e32 v[192:193], v[68:69]
	v_mov_b64_e32 v[196:197], v[68:69]
	v_cmp_ne_u32_e64 s[0:1], 0, v0
	v_cmp_eq_u32_e64 s[2:3], 0, v4
	s_add_i32 s80, s80, s11
	v_lshl_add_u32 v224, v198, 2, s4
	v_and_or_b32 v225, v11, 16, s30
	s_lshl_b32 s81, s31, 2
	v_lshlrev_b32_e32 v226, 2, v198
	v_mov_b32_e32 v227, 0x7f7f7f7f
	v_add_u32_e32 v228, 0, v3
	v_add_u32_e32 v229, 0, v2
	v_mov_b64_e32 v[70:71], v[66:67]
	v_mov_b64_e32 v[74:75], v[66:67]
	v_mov_b64_e32 v[78:79], v[66:67]
	v_mov_b64_e32 v[82:83], v[66:67]
	v_mov_b64_e32 v[86:87], v[66:67]
	v_mov_b64_e32 v[90:91], v[66:67]
	v_mov_b64_e32 v[94:95], v[66:67]
	v_mov_b64_e32 v[98:99], v[66:67]
	v_mov_b64_e32 v[102:103], v[66:67]
	v_mov_b64_e32 v[106:107], v[66:67]
	v_mov_b64_e32 v[110:111], v[66:67]
	v_mov_b64_e32 v[114:115], v[66:67]
	v_mov_b64_e32 v[118:119], v[66:67]
	v_mov_b64_e32 v[122:123], v[66:67]
	v_mov_b64_e32 v[126:127], v[66:67]
	v_mov_b64_e32 v[130:131], v[66:67]
	v_mov_b64_e32 v[134:135], v[66:67]
	v_mov_b64_e32 v[138:139], v[66:67]
	v_mov_b64_e32 v[142:143], v[66:67]
	v_mov_b64_e32 v[146:147], v[66:67]
	v_mov_b64_e32 v[150:151], v[66:67]
	v_mov_b64_e32 v[154:155], v[66:67]
	v_mov_b64_e32 v[158:159], v[66:67]
	v_mov_b64_e32 v[162:163], v[66:67]
	v_mov_b64_e32 v[166:167], v[66:67]
	v_mov_b64_e32 v[170:171], v[66:67]
	v_mov_b64_e32 v[174:175], v[66:67]
	v_mov_b64_e32 v[178:179], v[66:67]
	v_mov_b64_e32 v[182:183], v[66:67]
	v_mov_b64_e32 v[186:187], v[66:67]
	v_mov_b64_e32 v[190:191], v[66:67]
	v_mov_b64_e32 v[194:195], v[66:67]
	v_mov_b32_e32 v230, v210
	v_mov_b32_e32 v231, v204
	s_barrier
	s_branch .LBB0_2242

.LBB0_2487:
	s_add_u32 s28, s90, 0x3800000
	v_and_b32_e32 v11, 15, v0
	v_and_b32_e32 v13, 48, v0
	s_addc_u32 s29, s91, 0
	v_lshl_or_b32 v228, s0, 6, v11
	v_lshl_or_b32 v11, v11, 6, v13
	s_lshl_b32 s0, s0, 13
	v_and_b32_e32 v10, 32, v10
	v_bitop3_b32 v11, v11, s0, v10 bitop3:0xde
	s_lshl_b32 s0, s1, 5
	s_add_i32 s65, s15, 0x18000
	s_mov_b64 s[30:31], 0x80
	s_and_b32 s8, s0, 0x60
	v_lshlrev_b32_e32 v14, 6, v0
	s_movk_i32 s0, 0x3c0
	v_lshl_add_u64 v[8:9], v[8:9], 0, s[30:31]
	s_mov_b32 m0, s65
	s_add_i32 s66, s15, 0x1a000
	v_and_or_b32 v13, v14, s0, v13
	s_lshl_b32 s0, s8, 7
	s_waitcnt vmcnt(2)
	s_barrier
	global_load_lds_dwordx4 v[8:9], off
	v_lshl_add_u64 v[6:7], v[6:7], 0, s[30:31]
	s_mov_b32 m0, s66
	s_add_i32 s67, s15, 0x8000
	s_add_i32 s68, s15, 0xa000
	v_bitop3_b32 v10, s0, v13, v10 bitop3:0xf6
	global_load_lds_dwordx4 v[6:7], off
	v_lshl_add_u64 v[2:3], v[2:3], 0, s[30:31]
	s_mov_b32 m0, s67
	s_add_u32 s0, s24, 0x10080
	global_load_lds_dwordx4 v[2:3], off
	v_lshl_add_u64 v[2:3], v[4:5], 0, s[30:31]
	s_mov_b32 m0, s68
	s_addc_u32 s1, s25, 0
	s_add_i32 s70, s15, 0x1c000
	global_load_lds_dwordx4 v[2:3], off
	v_lshl_add_u64 v[2:3], s[0:1], 0, v[196:197]
	s_mov_b32 m0, s70
	s_add_i32 s71, s15, 0x1e000
	global_load_lds_dwordx4 v[2:3], off
	v_lshl_add_u64 v[2:3], s[0:1], 0, v[200:201]
	s_mov_b32 m0, s71
	s_and_b32 s6, s11, 0xc0
	global_load_lds_dwordx4 v[2:3], off
	s_cmpk_lt_u32 s11, 0x100
	s_cselect_b64 s[34:35], -1, 0
	s_ashr_i32 s7, s33, 8
	s_max_i32 s7, s7, 1
	s_add_i32 s7, s7, 0
	s_and_b64 s[4:5], s[4:5], exec
	s_cselect_b32 s72, s7, 2.0
	s_add_i32 s9, 0, 0x22400
	s_lshl_b32 s4, s6, 2
	s_lshl_b32 s11, s72, 8
	s_add_i32 s73, s9, s4
	s_add_i32 s74, s4, 0
	s_sub_i32 s4, s10, s11
	s_addk_i32 s4, 0x107
	s_ashr_i32 s75, s4, 3
	s_ashr_i32 s4, s97, 5
	s_ashr_i32 s5, s4, 31
	v_or_b32_e32 v208, s6, v198
	s_add_i32 s74, s74, 0x23000
	s_lshl_b64 s[6:7], s[4:5], 2
	s_waitcnt vmcnt(6)
	s_add_u32 s36, s90, s6
	v_mov_b32_e32 v68, v195
	v_mov_b32_e32 v69, v195
	v_lshrrev_b32_e32 v12, 1, v0
	v_and_b32_e32 v2, 16, v0
	s_addc_u32 s37, s91, s7
	s_mul_i32 s76, s75, s4
	s_add_i32 s4, 0, 0x22100
	v_mov_b32_e32 v66, v195
	v_mov_b32_e32 v67, v195
	v_mov_b64_e32 v[72:73], v[68:69]
	v_mov_b64_e32 v[76:77], v[68:69]
	v_mov_b64_e32 v[80:81], v[68:69]
	v_mov_b64_e32 v[84:85], v[68:69]
	v_mov_b64_e32 v[88:89], v[68:69]
	v_mov_b64_e32 v[92:93], v[68:69]
	v_mov_b64_e32 v[96:97], v[68:69]
	v_mov_b64_e32 v[100:101], v[68:69]
	v_mov_b64_e32 v[104:105], v[68:69]
	v_mov_b64_e32 v[108:109], v[68:69]
	v_mov_b64_e32 v[112:113], v[68:69]
	v_mov_b64_e32 v[116:117], v[68:69]
	v_mov_b64_e32 v[120:121], v[68:69]
	v_mov_b64_e32 v[124:125], v[68:69]
	v_mov_b64_e32 v[128:129], v[68:69]
	v_mov_b64_e32 v[132:133], v[68:69]
	v_mov_b64_e32 v[136:137], v[68:69]
	v_mov_b64_e32 v[140:141], v[68:69]
	v_mov_b64_e32 v[144:145], v[68:69]
	v_mov_b64_e32 v[148:149], v[68:69]
	v_mov_b64_e32 v[152:153], v[68:69]
	v_mov_b64_e32 v[156:157], v[68:69]
	v_mov_b64_e32 v[160:161], v[68:69]
	v_mov_b64_e32 v[164:165], v[68:69]
	v_mov_b64_e32 v[168:169], v[68:69]
	v_mov_b64_e32 v[172:173], v[68:69]
	v_mov_b64_e32 v[176:177], v[68:69]
	v_mov_b64_e32 v[180:181], v[68:69]
	v_mov_b64_e32 v[184:185], v[68:69]
	v_mov_b64_e32 v[188:189], v[68:69]
	v_mov_b64_e32 v[192:193], v[68:69]
	v_cmp_ne_u32_e64 s[0:1], 0, v0
	v_cmp_eq_u32_e64 s[2:3], 0, v2
	v_lshl_add_u32 v229, v1, 2, s9
	v_lshl_add_u32 v230, v199, 2, s9
	s_add_i32 s76, s76, s11
	v_lshl_add_u32 v231, v198, 2, s4
	v_and_or_b32 v232, v12, 16, s8
	v_lshl_add_u32 v233, v209, 2, s9
	v_lshl_add_u32 v234, v226, 2, s9
	v_mov_b32_e32 v235, 0x7f7f7f7f
	s_mov_b64 s[38:39], 0x100
	s_mov_b64 s[40:41], 0x180
	v_add_u32_e32 v236, 0, v10
	v_add_u32_e32 v237, 0, v11
	v_mov_b64_e32 v[70:71], v[66:67]
	v_mov_b64_e32 v[74:75], v[66:67]
	v_mov_b64_e32 v[78:79], v[66:67]
	v_mov_b64_e32 v[82:83], v[66:67]
	v_mov_b64_e32 v[86:87], v[66:67]
	v_mov_b64_e32 v[90:91], v[66:67]
	v_mov_b64_e32 v[94:95], v[66:67]
	v_mov_b64_e32 v[98:99], v[66:67]
	v_mov_b64_e32 v[102:103], v[66:67]
	v_mov_b64_e32 v[106:107], v[66:67]
	v_mov_b64_e32 v[110:111], v[66:67]
	v_mov_b64_e32 v[114:115], v[66:67]
	v_mov_b64_e32 v[118:119], v[66:67]
	v_mov_b64_e32 v[122:123], v[66:67]
	v_mov_b64_e32 v[126:127], v[66:67]
	v_mov_b64_e32 v[130:131], v[66:67]
	v_mov_b64_e32 v[134:135], v[66:67]
	v_mov_b64_e32 v[138:139], v[66:67]
	v_mov_b64_e32 v[142:143], v[66:67]
	v_mov_b64_e32 v[146:147], v[66:67]
	v_mov_b64_e32 v[150:151], v[66:67]
	v_mov_b64_e32 v[154:155], v[66:67]
	v_mov_b64_e32 v[158:159], v[66:67]
	v_mov_b64_e32 v[162:163], v[66:67]
	v_mov_b64_e32 v[166:167], v[66:67]
	v_mov_b64_e32 v[170:171], v[66:67]
	v_mov_b64_e32 v[174:175], v[66:67]
	v_mov_b64_e32 v[178:179], v[66:67]
	v_mov_b64_e32 v[182:183], v[66:67]
	v_mov_b64_e32 v[186:187], v[66:67]
	v_mov_b64_e32 v[190:191], v[66:67]
	v_mov_b32_e32 v210, v202
	v_mov_b32_e32 v212, v194
	s_barrier
	s_branch .LBB0_2490
